# cache policy: nt on the weight conversion's once-read f32 loads AND its bf16 output stores (stream beside the GEMM without evicting its L2 operands)
# speedup vs baseline: 1.0157x; 1.0157x over previous
; #define GAS __attribute__((address_space(1)))
; __device__ __forceinline__ unsigned pk2(float lo, float hi) { return f2bf(lo) | (f2bf(hi) << 16); }
; __device__ __forceinline__ void cvt_fin(const CvtD& d, int lane, const LAS unsigned char* buf, const LAS unsigned char* shb) {
;     ...
; #pragma unroll
;     for (int j = 0; j < 4; ++j) {
;         v4u o; o.x = pk2(v[j][0], v[j][1]); o.y = pk2(v[j][2], v[j][3]); o.z = pk2(v[j][4], v[j][5]); o.w = pk2(v[j][6], v[j][7]);
;         *(GAS v4u*)((GAS char*)(d.WT + ((size_t)((r0 >> 8) * d.KT + kb) * 256 + (r0 & 255) + 8 * j) * 64) + (unsigned)(nlo * 64 + 8 * c) * 2u) = o; }
.LBB0_982:
	s_ashr_i32 s17, s20, 8
	s_mul_i32 s17, s17, s34
	s_add_i32 s18, s17, s33
	s_ashr_i32 s19, s18, 31
	s_lshl_b32 s17, s20, 7
	s_add_i32 s16, s31, 1
	s_lshl_b64 s[18:19], s[18:19], 15
	s_and_b32 s17, s17, 0x7f80
	v_bfe_u32 v42, v36, 16, 1
	v_bfe_u32 v45, v38, 16, 1
	s_movk_i32 s21, 0x7fff
	s_add_u32 s14, s14, s18
	v_bfe_u32 v43, v40, 16, 1
	v_bfe_u32 v44, v30, 16, 1
	v_add3_u32 v38, v38, v45, s21
	v_add3_u32 v36, v36, v42, s21
	s_addc_u32 s15, s15, s19
	v_add3_u32 v30, v30, v44, s21
	v_add3_u32 v40, v40, v43, s21
	v_lshrrev_b32_e32 v42, 16, v36
	v_lshrrev_b32_e32 v36, 16, v38
	v_bfe_u32 v38, v39, 16, 1
	v_bfe_u32 v43, v31, 16, 1
	v_bfe_u32 v44, v41, 16, 1
	v_bfe_u32 v45, v37, 16, 1
	s_add_u32 s14, s14, s17
	v_lshrrev_b32_e32 v40, 16, v40
	v_lshrrev_b32_e32 v30, 16, v30
	v_add3_u32 v37, v37, v45, s21
	v_add3_u32 v41, v41, v44, s21
	v_add3_u32 v31, v31, v43, s21
	v_add3_u32 v38, v39, v38, s21
	s_addc_u32 s15, s15, 0
	v_and_or_b32 v38, v38, s76, v36
	v_and_or_b32 v36, v31, s76, v30
	v_and_or_b32 v39, v41, s76, v40
	v_and_or_b32 v37, v37, s76, v42
	v_lshl_add_u64 v[30:31], s[14:15], 0, v[8:9]
	global_store_dwordx4 v[30:31], v[36:39], off nt
	s_orn2_b64 s[14:15], s[8:9], exec
	s_nop 0
	v_bfe_u32 v36, v32, 16, 1
	v_bfe_u32 v37, v34, 16, 1
	v_bfe_u32 v38, v26, 16, 1
	v_bfe_u32 v39, v28, 16, 1
	v_add3_u32 v28, v28, v39, s21
	v_add3_u32 v26, v26, v38, s21
	v_add3_u32 v34, v34, v37, s21
	v_add3_u32 v32, v32, v36, s21
	v_bfe_u32 v36, v29, 16, 1
	v_bfe_u32 v37, v27, 16, 1
	v_bfe_u32 v38, v35, 16, 1
	v_bfe_u32 v39, v33, 16, 1
	v_lshrrev_b32_e32 v32, 16, v32
	v_lshrrev_b32_e32 v34, 16, v34
	v_lshrrev_b32_e32 v26, 16, v26
	v_lshrrev_b32_e32 v28, 16, v28
	v_add3_u32 v33, v33, v39, s21
	v_add3_u32 v35, v35, v38, s21
	v_add3_u32 v27, v27, v37, s21
	v_add3_u32 v29, v29, v36, s21
	v_and_or_b32 v28, v29, s76, v28
	v_and_or_b32 v26, v27, s76, v26
	v_and_or_b32 v29, v35, s76, v34
	v_and_or_b32 v27, v33, s76, v32
	global_store_dwordx4 v[30:31], v[26:29], off offset:1024 nt
	s_nop 1
	v_bfe_u32 v26, v22, 16, 1
	v_bfe_u32 v27, v24, 16, 1
	v_bfe_u32 v28, v18, 16, 1
	v_bfe_u32 v29, v20, 16, 1
	v_add3_u32 v20, v20, v29, s21
	v_add3_u32 v18, v18, v28, s21
	v_add3_u32 v24, v24, v27, s21
	v_add3_u32 v22, v22, v26, s21
	v_bfe_u32 v26, v21, 16, 1
	v_bfe_u32 v27, v19, 16, 1
	v_bfe_u32 v28, v25, 16, 1
	v_bfe_u32 v29, v23, 16, 1
	v_lshrrev_b32_e32 v22, 16, v22
	v_lshrrev_b32_e32 v24, 16, v24
	v_lshrrev_b32_e32 v18, 16, v18
	v_lshrrev_b32_e32 v20, 16, v20
	v_add3_u32 v23, v23, v29, s21
	v_add3_u32 v25, v25, v28, s21
	v_add3_u32 v19, v19, v27, s21
	v_add3_u32 v21, v21, v26, s21
	v_and_or_b32 v20, v21, s76, v20
	v_and_or_b32 v18, v19, s76, v18
	v_and_or_b32 v21, v25, s76, v24
	v_and_or_b32 v19, v23, s76, v22
	global_store_dwordx4 v[30:31], v[18:21], off offset:2048 nt
	s_nop 1
	v_bfe_u32 v18, v14, 16, 1
	v_bfe_u32 v19, v16, 16, 1
	v_bfe_u32 v20, v10, 16, 1
	v_bfe_u32 v21, v12, 16, 1
	v_add3_u32 v12, v12, v21, s21
	v_add3_u32 v10, v10, v20, s21
	v_add3_u32 v16, v16, v19, s21
	v_add3_u32 v14, v14, v18, s21
	v_bfe_u32 v18, v13, 16, 1
	v_bfe_u32 v19, v11, 16, 1
	v_bfe_u32 v20, v17, 16, 1
	v_bfe_u32 v21, v15, 16, 1
	v_lshrrev_b32_e32 v14, 16, v14
	v_lshrrev_b32_e32 v16, 16, v16
	v_lshrrev_b32_e32 v10, 16, v10
	v_lshrrev_b32_e32 v12, 16, v12
	v_add3_u32 v15, v15, v21, s21
	v_add3_u32 v17, v17, v20, s21
	v_add3_u32 v11, v11, v19, s21
	v_add3_u32 v13, v13, v18, s21
	v_and_or_b32 v12, v13, s76, v12
	v_and_or_b32 v10, v11, s76, v10
	v_and_or_b32 v13, v17, s76, v16
	v_and_or_b32 v11, v15, s76, v14
	global_store_dwordx4 v[30:31], v[10:13], off offset:3072 nt

; #define GAS __attribute__((address_space(1)))
; __device__ __forceinline__ unsigned pk2(float lo, float hi) { return f2bf(lo) | (f2bf(hi) << 16); }
; __device__ __forceinline__ void cvt_fin(const CvtD& d, int lane, const LAS unsigned char* buf, const LAS unsigned char* shb) {
;     ...
; #pragma unroll
;     for (int j = 0; j < 4; ++j) {
;         v4u o; o.x = pk2(v[j][0], v[j][1]); o.y = pk2(v[j][2], v[j][3]); o.z = pk2(v[j][4], v[j][5]); o.w = pk2(v[j][6], v[j][7]);
;         *(GAS v4u*)((GAS char*)(d.WT + ((size_t)((r0 >> 8) * d.KT + kb) * 256 + (r0 & 255) + 8 * j) * 64) + (unsigned)(nlo * 64 + 8 * c) * 2u) = o; }
.LBB0_1083:
	s_ashr_i32 s14, s18, 8
	s_mul_i32 s14, s14, s31
	s_add_i32 s14, s14, s23
	s_ashr_i32 s15, s14, 31
	s_lshl_b32 s16, s18, 7
	s_lshl_b64 s[14:15], s[14:15], 15
	s_and_b32 s16, s16, 0x7f80
	v_bfe_u32 v42, v36, 16, 1
	v_bfe_u32 v45, v38, 16, 1
	s_movk_i32 s17, 0x7fff
	s_add_u32 s12, s12, s14
	v_bfe_u32 v43, v40, 16, 1
	v_bfe_u32 v44, v30, 16, 1
	v_add3_u32 v38, v38, v45, s17
	v_add3_u32 v36, v36, v42, s17
	s_addc_u32 s13, s13, s15
	v_add3_u32 v30, v30, v44, s17
	v_add3_u32 v40, v40, v43, s17
	v_lshrrev_b32_e32 v42, 16, v36
	v_lshrrev_b32_e32 v36, 16, v38
	v_bfe_u32 v38, v39, 16, 1
	v_bfe_u32 v43, v31, 16, 1
	v_bfe_u32 v44, v41, 16, 1
	v_bfe_u32 v45, v37, 16, 1
	s_add_u32 s12, s12, s16
	v_lshrrev_b32_e32 v40, 16, v40
	v_lshrrev_b32_e32 v30, 16, v30
	v_add3_u32 v37, v37, v45, s17
	v_add3_u32 v41, v41, v44, s17
	v_add3_u32 v31, v31, v43, s17
	v_add3_u32 v38, v39, v38, s17
	s_addc_u32 s13, s13, 0
	v_and_or_b32 v38, v38, s76, v36
	v_and_or_b32 v36, v31, s76, v30
	v_and_or_b32 v39, v41, s76, v40
	v_and_or_b32 v37, v37, s76, v42
	v_lshl_add_u64 v[30:31], s[12:13], 0, v[8:9]
	global_store_dwordx4 v[30:31], v[36:39], off nt
	s_mov_b64 s[14:15], -1
	v_readfirstlane_b32 s16, v0
	v_bfe_u32 v36, v32, 16, 1
	v_bfe_u32 v37, v34, 16, 1
	v_bfe_u32 v38, v26, 16, 1
	v_bfe_u32 v39, v28, 16, 1
	v_add3_u32 v28, v28, v39, s17
	v_add3_u32 v26, v26, v38, s17
	v_add3_u32 v34, v34, v37, s17
	v_add3_u32 v32, v32, v36, s17
	v_bfe_u32 v36, v29, 16, 1
	v_bfe_u32 v37, v27, 16, 1
	v_bfe_u32 v38, v35, 16, 1
	v_bfe_u32 v39, v33, 16, 1
	v_lshrrev_b32_e32 v32, 16, v32
	v_lshrrev_b32_e32 v34, 16, v34
	v_lshrrev_b32_e32 v26, 16, v26
	v_lshrrev_b32_e32 v28, 16, v28
	v_add3_u32 v33, v33, v39, s17
	v_add3_u32 v35, v35, v38, s17
	v_add3_u32 v27, v27, v37, s17
	v_add3_u32 v29, v29, v36, s17
	v_and_or_b32 v28, v29, s76, v28
	v_and_or_b32 v26, v27, s76, v26
	v_and_or_b32 v29, v35, s76, v34
	v_and_or_b32 v27, v33, s76, v32
	global_store_dwordx4 v[30:31], v[26:29], off offset:1024 nt
	s_nop 1
	v_bfe_u32 v26, v22, 16, 1
	v_bfe_u32 v27, v24, 16, 1
	v_bfe_u32 v28, v18, 16, 1
	v_bfe_u32 v29, v20, 16, 1
	v_add3_u32 v20, v20, v29, s17
	v_add3_u32 v18, v18, v28, s17
	v_add3_u32 v24, v24, v27, s17
	v_add3_u32 v22, v22, v26, s17
	v_bfe_u32 v26, v21, 16, 1
	v_bfe_u32 v27, v19, 16, 1
	v_bfe_u32 v28, v25, 16, 1
	v_bfe_u32 v29, v23, 16, 1
	v_lshrrev_b32_e32 v22, 16, v22
	v_lshrrev_b32_e32 v24, 16, v24
	v_lshrrev_b32_e32 v18, 16, v18
	v_lshrrev_b32_e32 v20, 16, v20
	v_add3_u32 v23, v23, v29, s17
	v_add3_u32 v25, v25, v28, s17
	v_add3_u32 v19, v19, v27, s17
	v_add3_u32 v21, v21, v26, s17
	v_and_or_b32 v20, v21, s76, v20
	v_and_or_b32 v18, v19, s76, v18
	v_and_or_b32 v21, v25, s76, v24
	v_and_or_b32 v19, v23, s76, v22
	global_store_dwordx4 v[30:31], v[18:21], off offset:2048 nt
	s_nop 1
	v_bfe_u32 v18, v14, 16, 1
	v_bfe_u32 v19, v16, 16, 1
	v_bfe_u32 v20, v10, 16, 1
	v_bfe_u32 v21, v12, 16, 1
	v_add3_u32 v12, v12, v21, s17
	v_add3_u32 v10, v10, v20, s17
	v_add3_u32 v16, v16, v19, s17
	v_add3_u32 v14, v14, v18, s17
	v_bfe_u32 v18, v13, 16, 1
	v_bfe_u32 v19, v11, 16, 1
	v_bfe_u32 v20, v17, 16, 1
	v_bfe_u32 v21, v15, 16, 1
	v_lshrrev_b32_e32 v14, 16, v14
	v_lshrrev_b32_e32 v16, 16, v16
	v_lshrrev_b32_e32 v10, 16, v10
	v_lshrrev_b32_e32 v12, 16, v12
	v_add3_u32 v15, v15, v21, s17
	v_add3_u32 v17, v17, v20, s17
	v_add3_u32 v11, v11, v19, s17
	v_add3_u32 v13, v13, v18, s17
	v_and_or_b32 v12, v13, s76, v12
	v_and_or_b32 v10, v11, s76, v10
	v_and_or_b32 v13, v17, s76, v16
	v_and_or_b32 v11, v15, s76, v14
	global_store_dwordx4 v[30:31], v[10:13], off offset:3072 nt
	s_and_saveexec_b64 s[12:13], s[8:9]
	s_cbranch_execz .LBB0_983
	s_add_i32 s31, s22, 1
	s_cmp_lg_u32 s31, 8
	s_cbranch_scc1 .LBB0_1093
	v_cmp_gt_i32_e32 vcc, s26, v78
	s_and_saveexec_b64 s[8:9], vcc
	s_cbranch_execz .LBB0_1089
	s_and_saveexec_b64 s[14:15], s[2:3]
	s_cbranch_execz .LBB0_1088
	global_atomic_add v5, v[2:3], v234, off sc0
